# attn: key-tile rotation (6qb+13head)&31
# baseline (speedup 1.0000x reference)
.Lp_top:
	s_lshl_b32 s6, s21, 20
	s_add_u32 s4, s4, s6
	s_addc_u32 s5, s5, 0
	v_lshlrev_b32_e32 v54, 4, v0
	v_mov_b32_e32 v55, v63
	s_mul_i32 s3, s3, 6
	s_mul_i32 s20, s21, 13
	v_lshl_add_u64 v[4:5], s[4:5], 0, v[54:55]
	s_mov_b64 s[4:5], 0x1000000
	s_add_i32 s20, s20, s3
	v_lshl_add_u64 v[170:171], v[4:5], 0, s[4:5]
	s_and_b32 s22, s20, 31
	s_lshl_b32 s4, s20, 12
	s_lshl_b32 s12, s22, 13
	s_add_i32 s5, s4, 0x1000
	v_lshl_add_u64 v[58:59], v[170:171], 0, s[12:13]
	s_mov_b32 s3, 0x80000
	s_and_b32 s5, s5, 0x1f000
	v_add_co_u32_e32 v16, vcc, s3, v58
	s_lshl_b32 s12, s5, 1
	s_nop 0
	v_addc_co_u32_e32 v17, vcc, 0, v59, vcc
	v_lshl_add_u64 v[56:57], v[170:171], 0, s[12:13]
	global_load_dwordx4 v[4:7], v[58:59], off
	global_load_dwordx4 v[8:11], v[56:57], off
	global_load_dwordx4 v[12:15], v[16:17], off
	v_add_co_u32_e32 v16, vcc, s3, v56
	v_lshrrev_b32_e32 v184, 8, v0
	s_nop 0
	v_addc_co_u32_e32 v17, vcc, 0, v57, vcc
	global_load_dwordx4 v[16:19], v[16:17], off
	v_and_b32_e32 v20, 19, v0
	v_lshlrev_b32_e32 v21, 1, v0
	v_and_b32_e32 v2, 4, v2
	v_and_or_b32 v20, v21, 8, v20
	v_lshlrev_b32_e32 v101, 5, v184
	s_addk_i32 s4, 0x2000
	v_or3_b32 v2, v20, v2, v101
	s_and_b32 s4, s4, 0x1f000
	v_mul_u32_u24_e32 v2, 0x48, v2
	s_lshl_b32 s12, s4, 1
	v_lshlrev_b32_e32 v3, 3, v0
	v_lshlrev_b32_e32 v100, 1, v99
	v_lshlrev_b32_e32 v2, 1, v2
	v_lshl_add_u64 v[60:61], v[170:171], 0, s[12:13]
	v_and_b32_e32 v3, 56, v3
	v_add3_u32 v186, 0, v2, v100
	v_add_co_u32_e32 v2, vcc, s3, v60
	v_lshlrev_b32_e32 v68, 1, v3
	s_nop 0
	v_addc_co_u32_e32 v3, vcc, 0, v61, vcc
	global_load_dwordx4 v[162:165], v[60:61], off
	global_load_dwordx4 v[166:169], v[2:3], off
	v_lshrrev_b32_e32 v82, 3, v0
	v_mul_u32_u24_e32 v22, 0x48, v82
	v_lshlrev_b32_e32 v21, 1, v22
	v_add3_u32 v185, 0, v21, v68
	s_mov_b64 s[24:25], 0x80000
	s_add_i32 s17, s20, 3
	s_add_i32 s18, s20, 4
	v_mov_b32_e32 v62, v63
	v_lshrrev_b32_e32 v55, 6, v0
	v_mov_b32_e32 v83, 0
	v_mov_b32_e32 v84, 0
	v_lshl_add_u64 v[70:71], v[58:59], 0, s[24:25]
	v_lshl_add_u64 v[66:67], v[56:57], 0, s[24:25]
	v_lshl_add_u64 v[64:65], v[60:61], 0, s[24:25]
	s_waitcnt vmcnt(5)
	ds_write_b128 v185, v[4:7]
	s_waitcnt vmcnt(3)
	ds_write_b128 v185, v[12:15] offset:9216
	ds_write_b128 v185, v[8:11] offset:18432
	s_waitcnt vmcnt(2)
	ds_write_b128 v185, v[16:19] offset:27648
	s_waitcnt lgkmcnt(0)
	s_barrier
	ds_read_b128 v[2:5], v186
	ds_read_b128 v[38:41], v186 offset:32
	s_waitcnt lgkmcnt(1)
	v_mfma_f32_32x32x16_f16 v[2:17], v[2:5], v[114:117], 0
	ds_read_b128 v[18:21], v186 offset:9216
	ds_read_b128 v[46:49], v186 offset:9248
	s_waitcnt lgkmcnt(1)
	v_mfma_f32_32x32x16_f16 v[18:33], v[18:21], v[130:133], 0
	v_mfma_f32_32x32x16_f16 v[2:17], v[38:41], v[118:121], v[2:17]
	s_waitcnt lgkmcnt(0)
	v_mfma_f32_32x32x16_f16 v[18:33], v[46:49], v[134:137], v[18:33]
	ds_read_b128 v[38:41], v186 offset:64
	ds_read_b128 v[46:49], v186 offset:96
	s_waitcnt lgkmcnt(1)
	v_mfma_f32_32x32x16_f16 v[2:17], v[38:41], v[122:125], v[2:17]
	ds_read_b128 v[38:41], v186 offset:9280
	ds_read_b128 v[50:53], v186 offset:9312
	s_load_dwordx4 s[4:7], s[0:1], 0x38
	s_load_dwordx2 s[14:15], s[0:1], 0x8
	s_mov_b32 s0, -2
	s_mov_b32 s1, 0x3f800000
	s_waitcnt lgkmcnt(0)
	s_barrier
	v_mfma_f32_32x32x16_f16 v[18:33], v[38:41], v[138:141], v[18:33]
	v_mfma_f32_32x32x16_f16 v[2:17], v[46:49], v[126:129], v[2:17]
	v_mfma_f32_32x32x16_f16 v[18:33], v[50:53], v[142:145], v[18:33]
	s_lshl_b32 s12, s17, 13
	s_and_b32 s12, s12, 0x3e000
	s_add_u32 s28, s12, s3
	s_mov_b32 s29, 0
	v_lshl_add_u64 v[176:177], v[170:171], 0, s[12:13]
	global_load_dwordx4 v[50:53], v[176:177], off
	v_lshl_add_u64 v[176:177], v[170:171], 0, s[28:29]
	global_load_dwordx4 v[94:97], v[176:177], off
	s_nop 7
	s_cmp_eq_u32 s37, 1
	s_cbranch_scc0 .Lf_A
	v_mov_b32_e32 v83, 0xf149f2ca
	v_mov_b32_e32 v84, 0xf149f2ca
	s_branch .Ls_A

.Ll1_cont:
	ds_bpermute_b32 v2, v69, v84
	ds_bpermute_b32 v5, v69, v83
	v_max_f32_e32 v4, v84, v84
	v_max_f32_e32 v7, v83, v83
	ds_bpermute_b32 v3, v69, v63
	s_waitcnt lgkmcnt(2)
	v_max_f32_e32 v6, v2, v2
	v_max_f32_e32 v4, v4, v6
	v_sub_f32_e32 v6, v84, v4
	v_exp_f32_e32 v9, v6
	s_waitcnt lgkmcnt(1)
	v_max_f32_e32 v6, v5, v5
	v_sub_f32_e32 v2, v2, v4
	v_max_f32_e32 v6, v7, v6
	v_exp_f32_e32 v11, v2
	ds_bpermute_b32 v2, v69, v62
	v_sub_f32_e32 v5, v5, v6
	v_sub_f32_e32 v7, v83, v6
	v_exp_f32_e32 v10, v5
	v_exp_f32_e32 v8, v7
	v_cmp_gt_u32_e32 vcc, 32, v98
	s_waitcnt lgkmcnt(0)
	v_pk_mul_f32 v[2:3], v[10:11], v[2:3]
	s_nop 0
	v_pk_fma_f32 v[8:9], v[62:63], v[8:9], v[2:3]
	v_lshlrev_b32_e32 v2, 7, v184
	v_or3_b32 v10, v183, v2, v1
	s_and_saveexec_b64 s[0:1], vcc
	v_lshl_add_u32 v2, v10, 4, 0
	v_add_u32_e32 v2, 0x21000, v2
	v_mov_b32_e32 v5, v9
	v_mov_b32_e32 v7, v8
	ds_write_b128 v2, v[4:7]
	s_or_b64 exec, exec, s[0:1]
	s_lshl_b32 s12, s21, 7
	s_mov_b32 s3, 0
	v_or_b32_e32 v2, s12, v82
	s_lshl_b32 s13, s21, 11
	s_add_i32 s23, 0, 0x12000
	v_lshlrev_b32_e32 v2, 12, v2
	v_mov_b32_e32 v3, 0
	s_add_i32 s13, s13, s16
	s_lshl_b64 s[0:1], s[2:3], 13
	v_lshl_add_u64 v[12:13], s[14:15], 0, v[2:3]
	v_mov_b32_e32 v69, v3
	s_add_u32 s0, s10, s0
	v_lshl_add_u64 v[172:173], v[12:13], 0, v[68:69]
	s_addc_u32 s1, s11, s1
	s_lshl_b32 s10, s22, 7
	s_mov_b32 s11, s3
	s_waitcnt vmcnt(1)
	v_lshl_add_u64 v[36:37], v[172:173], 0, s[10:11]
	s_mov_b32 s10, 0x40000
	v_add_co_u32_e32 v38, vcc, s10, v36
	s_waitcnt lgkmcnt(0)
	s_barrier
	global_load_dwordx4 v[12:15], v[58:59], off
	global_load_dwordx4 v[16:19], v[70:71], off
	v_addc_co_u32_e32 v39, vcc, 0, v37, vcc
	global_load_dwordx4 v[20:23], v[56:57], off
	global_load_dwordx4 v[24:27], v[66:67], off
	global_load_dwordx4 v[28:31], v[36:37], off
	global_load_dwordx4 v[32:35], v[38:39], off
	v_add_f32_e32 v2, v78, v80
	s_movk_i32 s11, 0x1200
	v_add_f32_e32 v5, v79, v81
	s_mov_b32 s14, 0x3fb8aa3b
	v_lshlrev_b32_e32 v10, 4, v10
	v_mov_b32_e32 v36, s23
	v_mul_f32_e32 v37, 0x3fb8aa3b, v2
	v_mul_f32_e32 v38, 0x3fb8aa3b, v5
	v_xor_b32_e32 v10, 0x800, v10
	v_mad_u32_u24 v40, v55, s11, v36
	v_fma_f32 v36, v2, s14, -v37
	v_rndne_f32_e32 v39, v37
	v_fma_f32 v41, v5, s14, -v38
	s_waitcnt vmcnt(6)
	v_rndne_f32_e32 v42, v38
	v_add_u32_e32 v10, 0, v10
	v_fmac_f32_e32 v36, 0x32a5705f, v2
	v_sub_f32_e32 v37, v37, v39
	v_fmac_f32_e32 v41, 0x32a5705f, v5
	v_sub_f32_e32 v38, v38, v42
	v_add_u32_e32 v10, 0x21000, v10
	v_add_f32_e32 v44, v37, v36
	global_load_dwordx4 v[146:149], v[60:61], off
	global_load_dwordx4 v[150:153], v[64:65], off
	v_cvt_i32_f32_e32 v43, v39
	v_add_f32_e32 v41, v38, v41
	ds_read_b128 v[36:39], v10
	v_exp_f32_e32 v10, v44
	v_cvt_i32_f32_e32 v42, v42
	v_exp_f32_e32 v41, v41
	s_mov_b32 s21, 0xc2ce8ed0
	s_lshl_b32 s11, s20, 6
	s_add_i32 s14, s11, 64
	v_ldexp_f32 v10, v10, v43
	v_cmp_ngt_f32_e32 vcc, s21, v2
	s_mov_b32 s22, 0x42b17218
	s_and_b32 s14, s14, 0x7c0
	v_ldexp_f32 v41, v41, v42
	v_cndmask_b32_e32 v10, 0, v10, vcc
	v_cmp_ngt_f32_e32 vcc, s21, v5
	v_mov_b32_e32 v7, 0x7f800000
	v_max_f32_e32 v11, v4, v4
	s_mov_b32 s15, s3
	s_lshl_b32 s14, s14, 1
	s_waitcnt lgkmcnt(0)
	v_max_f32_e32 v42, v36, v36
	v_cndmask_b32_e32 v41, 0, v41, vcc
	v_cmp_nlt_f32_e32 vcc, s22, v2
	v_max_f32_e32 v187, v11, v42
	v_mov_b32_e32 v55, v3
	v_cndmask_b32_e32 v2, v7, v10, vcc
	v_cmp_nlt_f32_e32 vcc, s22, v5
	v_lshl_add_u64 v[10:11], v[172:173], 0, s[14:15]
	v_lshl_add_u64 v[178:179], s[0:1], 0, v[54:55]
	v_cndmask_b32_e32 v5, v7, v41, vcc
	v_sub_f32_e32 v2, v2, v5
	v_add_f32_e32 v41, 0x3e4ccccd, v2
	v_sub_f32_e32 v2, v4, v187
	v_max_f32_e32 v4, v6, v6
	s_and_b32 s1, s2, 7
	s_mulk_i32 s1, 0x680
	s_mulk_i32 s19, 0x340
	s_add_i32 s0, s20, 2
	s_waitcnt vmcnt(7)
	ds_write_b128 v185, v[12:15]
	s_waitcnt vmcnt(6)
	ds_write_b128 v185, v[16:19] offset:9216
	s_waitcnt vmcnt(5)
	ds_write_b128 v185, v[20:23] offset:18432
	s_waitcnt vmcnt(4)
	ds_write_b128 v185, v[24:27] offset:27648
	s_waitcnt vmcnt(3)
	ds_write_b128 v185, v[28:31] offset:36864
	s_waitcnt vmcnt(2)
	ds_write_b128 v185, v[32:35] offset:46080
	v_add_co_u32_e32 v12, vcc, s10, v10
	v_exp_f32_e32 v23, v2
	s_nop 0
	v_addc_co_u32_e32 v13, vcc, 0, v11, vcc
	global_load_dwordx4 v[154:157], v[10:11], off
	global_load_dwordx4 v[158:161], v[12:13], off
	s_waitcnt lgkmcnt(0)
	s_barrier
	ds_read_b128 v[10:13], v186
	v_sub_f32_e32 v2, v36, v187
	v_exp_f32_e32 v25, v2
	v_max_f32_e32 v2, v38, v38
	v_max_f32_e32 v188, v4, v2
	v_sub_f32_e32 v2, v6, v188
	v_exp_f32_e32 v22, v2
	v_sub_f32_e32 v2, v38, v188
	v_exp_f32_e32 v24, v2
	ds_read_b128 v[14:17], v186 offset:9216
	ds_read_b128 v[18:21], v186 offset:32
	s_waitcnt lgkmcnt(2)
	v_mfma_f32_32x32x16_f16 v[66:81], v[10:13], v[114:117], 0
	v_mov_b32_e32 v36, v39
	v_mul_f32_e64 v10, v36, v24
	v_mul_f32_e64 v11, v37, v25
	ds_read_b128 v[4:7], v186 offset:9248
	s_add_i32 s1, s1, s19
	s_lshr_b32 s28, s2, 4
	s_mulk_i32 s28, 0x100
	s_add_i32 s1, s1, s28
	s_mov_b32 s14, 0x30000
	s_mov_b32 s15, 0x80000
	s_mov_b32 s19, 0
	s_waitcnt lgkmcnt(2)
	v_mfma_f32_32x32x16_f16 v[82:97], v[14:17], v[130:133], 0
	v_fma_f32 v16, v8, v22, v10
	v_fma_f32 v17, v9, v23, v11
	v_log_f32_e32 v238, v17
	s_nop 0
	v_add_f32_e32 v187, v187, v238
	v_sub_f32_e32 v240, 0, v187
	v_sub_f32_e32 v241, 0, v187
	v_sub_f32_e32 v242, 0, v187
	v_sub_f32_e32 v243, 0, v187
	v_sub_f32_e32 v244, 0, v187
	v_sub_f32_e32 v245, 0, v187
	v_sub_f32_e32 v246, 0, v187
	v_sub_f32_e32 v247, 0, v187
	v_sub_f32_e32 v248, 0, v187
	v_sub_f32_e32 v249, 0, v187
	v_sub_f32_e32 v250, 0, v187
	v_sub_f32_e32 v251, 0, v187
	v_sub_f32_e32 v252, 0, v187
	v_sub_f32_e32 v253, 0, v187
	v_sub_f32_e32 v254, 0, v187
	v_sub_f32_e32 v255, 0, v187
	v_lshrrev_b32_e32 v22, 3, v98
	v_or3_b32 v2, s13, v183, v22
	v_lshlrev_b64 v[8:9], 13, v[2:3]
	v_lshl_add_u64 v[8:9], s[4:5], 0, v[8:9]
	v_lshlrev_b32_e32 v2, 2, v101
	v_lshl_add_u64 v[8:9], v[8:9], 0, v[2:3]
	v_and_b32_e32 v2, 0x70, v54
	v_lshl_add_u64 v[174:175], v[8:9], 0, v[2:3]
	ds_read_b128 v[8:11], v186 offset:64
	s_waitcnt lgkmcnt(2)
	v_mfma_f32_32x32x16_f16 v[66:81], v[18:21], v[118:121], v[66:81]
	v_div_scale_f32 v18, s[4:5], v16, v16, -v41
	v_rcp_f32_e32 v19, v18
	v_div_scale_f32 v20, vcc, -v41, v16, -v41
	s_mov_b32 s13, 0x20000
	v_mov_b32_e32 v24, v3
	s_waitcnt lgkmcnt(1)
	v_mfma_f32_32x32x16_f16 v[82:97], v[4:7], v[134:137], v[82:97]
	v_fma_f32 v4, -v18, v19, 1.0
	v_fmac_f32_e32 v19, v4, v19
	v_mul_f32_e32 v21, v20, v19
	ds_read_b128 v[4:7], v186 offset:9280
	ds_read_b128 v[12:15], v186 offset:96
	v_mov_b32_e32 v25, v3
	v_mov_b32_e32 v26, v3
	v_mov_b32_e32 v27, v3
	s_waitcnt lgkmcnt(2)
	v_mfma_f32_32x32x16_f16 v[66:81], v[8:11], v[122:125], v[66:81]
	v_fma_f32 v8, -v18, v21, v20
	v_fmac_f32_e32 v21, v8, v19
	v_fma_f32 v18, -v18, v21, v20
	v_div_scale_f32 v20, s[4:5], v17, v17, 1.0
	v_rcp_f32_e32 v23, v20
	ds_read_b128 v[8:11], v186 offset:9312
	s_waitcnt lgkmcnt(2)
	v_mfma_f32_32x32x16_f16 v[82:97], v[4:7], v[138:141], v[82:97]
	v_div_fmas_f32 v4, v18, v19, v21
	v_div_fixup_f32 v176, v4, v16, -v41
	v_fma_f32 v4, -v20, v23, 1.0
	v_fmac_f32_e32 v23, v4, v23
	v_div_scale_f32 v4, vcc, 1.0, v17, 1.0
	v_mul_f32_e32 v5, v4, v23
	v_fma_f32 v6, -v20, v5, v4
	v_fmac_f32_e32 v5, v6, v23
	s_waitcnt lgkmcnt(1)
	v_mfma_f32_32x32x16_f16 v[66:81], v[12:15], v[126:129], v[66:81]
	v_fma_f32 v4, -v20, v5, v4
	v_div_fmas_f32 v4, v4, v23, v5
	v_div_fixup_f32 v177, v4, v17, 1.0
	v_mul_u32_u24_e32 v4, 0x90, v22
	v_add3_u32 v189, v40, v4, v2
	v_mul_u32_u24_e32 v2, 0x90, v1
	v_lshlrev_b32_e32 v4, 2, v99
	s_waitcnt lgkmcnt(0)
	v_mfma_f32_32x32x16_f16 v[82:97], v[8:11], v[142:145], v[82:97]
	v_add3_u32 v190, v40, v2, v4
	v_mul_u32_u24_e32 v2, 0x48, v1
	v_lshl_add_u32 v2, v2, 1, 0
	v_lshlrev_b32_e32 v4, 1, v101
	v_add3_u32 v191, v2, v4, v100
	s_mov_b32 s4, 0x3f800000
	s_mov_b32 s5, 0x10000
	v_mov_b32_e32 v2, v3
	v_mov_b32_e32 v4, v3
	v_mov_b32_e32 v5, v3
	v_mov_b32_e32 v6, v3
	v_mov_b32_e32 v7, v3
	v_mov_b32_e32 v8, v3
	v_mov_b32_e32 v9, v3
	v_mov_b32_e32 v10, v3
	v_mov_b32_e32 v11, v3
	v_mov_b32_e32 v12, v3
	v_mov_b32_e32 v13, v3
	v_mov_b32_e32 v14, v3
	v_mov_b32_e32 v15, v3
	v_mov_b32_e32 v16, v3
	v_mov_b32_e32 v17, v3
	v_mov_b32_e32 v18, v3
	v_mov_b32_e32 v19, v3
	v_mov_b32_e32 v20, v3
	v_mov_b32_e32 v21, v3
	v_mov_b32_e32 v22, v3
	v_mov_b32_e32 v23, v3
	v_mov_b32_e32 v28, v3
	v_mov_b32_e32 v29, v3
	v_mov_b32_e32 v30, v3
	v_mov_b32_e32 v31, v3
	v_mov_b32_e32 v32, v3
	v_mov_b32_e32 v33, v3
	v_mov_b32_e32 v34, v3
	v_mov_b32_e32 v35, v3
	v_mov_b32_e32 v36, v3
	v_mov_b32_e32 v37, v3
	v_mov_b32_e32 v38, v3
	v_mov_b32_e32 v39, v3
	v_mov_b32_e32 v40, v3
	v_mov_b32_e32 v41, v3
	v_mov_b32_e32 v42, v3
	v_mov_b32_e32 v43, v3
	v_mov_b32_e32 v44, v3
	v_mov_b32_e32 v45, v3
	v_mov_b32_e32 v46, v3
	v_mov_b32_e32 v47, v3
	v_mov_b32_e32 v48, v3
	v_mov_b32_e32 v49, v3
	v_mov_b32_e32 v50, v3
	v_mov_b32_e32 v51, v3
	v_mov_b32_e32 v52, v3
	v_mov_b32_e32 v53, v3
	v_mov_b32_e32 v54, v3
	v_mov_b32_e32 v56, v3
	v_mov_b32_e32 v57, v3
	v_mov_b32_e32 v58, v3
	v_mov_b32_e32 v59, v3
	v_mov_b32_e32 v60, v3
	v_mov_b32_e32 v61, v3
	v_mov_b32_e32 v62, v3
	v_mov_b32_e32 v63, v3
	v_mov_b32_e32 v64, v3
	v_mov_b32_e32 v65, v3
	v_add_u32_e32 v192, 0xd800, v191
	v_sub_f32_e32 v66, v66, v187
	v_sub_f32_e32 v67, v67, v187
	v_sub_f32_e32 v68, v68, v187
	v_sub_f32_e32 v69, v69, v187
	v_sub_f32_e32 v70, v70, v187
	v_sub_f32_e32 v71, v71, v187
	v_sub_f32_e32 v72, v72, v187
	v_sub_f32_e32 v73, v73, v187
	v_sub_f32_e32 v74, v74, v187
	v_sub_f32_e32 v75, v75, v187
	v_sub_f32_e32 v76, v76, v187
	v_sub_f32_e32 v77, v77, v187
	v_sub_f32_e32 v78, v78, v187
	v_sub_f32_e32 v79, v79, v187
	v_sub_f32_e32 v80, v80, v187
	v_sub_f32_e32 v81, v81, v187
	s_mov_b32 s27, 0x42c80000
	v_cmp_gt_f32_e64 vcc, |v188|, s27
	s_cbranch_vccnz .Ll2_gen
	v_sub_f32_e32 v238, 0, v188
	v_exp_f32_e32 v238, v238
	s_nop 0
	v_mul_f32_e32 v176, v176, v238
	s_barrier
	s_branch .Ll2f_top
